# speedup vs baseline: 1.0076x; 1.0076x over previous
.LBB1_3:
	s_mul_i32 s0, s7, s2
	s_sub_i32 s0, s6, s0
	s_add_i32 s1, s7, 1
	s_sub_i32 s6, s0, s2
	s_cmp_ge_u32 s0, s2
	s_cselect_b32 s1, s1, s7
	s_cselect_b32 s0, s6, s0
	s_add_i32 s6, s1, 1
	s_cmp_ge_u32 s0, s2
	s_cselect_b32 s0, s6, s1
	s_xor_b32 s0, s0, s5
	s_sub_i32 s0, s0, s5
	s_mul_i32 s79, s0, s76
	s_add_i32 s0, s79, s0
	s_lshl_b32 s33, s59, 7
	s_add_i32 s4, s33, s4
	s_min_i32 s80, s0, s3
	s_mul_i32 s0, s72, 0x4080
	s_mul_hi_i32 s1, s72, 0x4080
	s_add_u32 s0, s62, s0
	s_addc_u32 s1, s63, s1
	s_mul_i32 s2, s79, 0x4080
	v_and_b32_e32 v114, 63, v0
	s_mul_hi_i32 s3, s79, 0x4080
	s_add_u32 s2, s0, s2
	s_addc_u32 s3, s1, s3
	v_lshlrev_b32_e32 v108, 4, v114
	v_lshl_add_u64 v[2:3], s[2:3], 0, v[108:109]
	s_ashr_i32 s2, s4, 5
	s_mul_hi_i32 s3, s2, 0x4080
	s_mulk_i32 s2, 0x4080
	v_lshrrev_b32_e32 v27, 6, v0
	s_add_u32 s2, s62, s2
	s_addc_u32 s3, s63, s3
	v_lshlrev_b32_e32 v6, 10, v27
	v_lshl_add_u64 v[4:5], s[2:3], 0, v[108:109]
	v_mov_b32_e32 v7, v109
	v_lshl_add_u64 v[8:9], v[2:3], 0, v[6:7]
	v_lshl_add_u64 v[10:11], v[4:5], 0, v[6:7]
	v_add_u32_e32 v14, 0x3000, v6
	v_add_u32_e32 v16, 0x6000, v6
	v_add_u32_e32 v18, 0x9000, v6
	v_bfe_u32 v119, v0, 6, 2
	v_and_b32_e32 v118, 31, v0
	s_mov_b64 s[62:63], 0xc00
	v_add_u32_e32 v15, 0x15000, v6
	s_mov_b64 s[2:3], 0xc00
	v_lshl_add_u64 v[12:13], v[10:11], 0, s[2:3]
	v_readfirstlane_b32 s4, v15
	s_mov_b32 m0, s4
	s_nop 0
	global_load_lds_dwordx4 v[12:13], off
	v_add_u32_e32 v15, 0x18000, v6
	s_mov_b64 s[2:3], 0x3c00
	v_lshl_add_u64 v[12:13], v[10:11], 0, s[2:3]
	v_readfirstlane_b32 s4, v15
	s_mov_b32 m0, s4
	s_nop 0
	global_load_lds_dwordx4 v[12:13], off
	v_add_u32_e32 v15, 0x1b000, v6
	s_mov_b64 s[2:3], 0x6c00
	v_lshl_add_u64 v[12:13], v[10:11], 0, s[2:3]
	v_readfirstlane_b32 s4, v15
	s_mov_b32 m0, s4
	s_nop 0
	global_load_lds_dwordx4 v[12:13], off
	v_add_u32_e32 v15, 0x1e000, v6
	s_mov_b64 s[2:3], 0x9c00
	v_lshl_add_u64 v[12:13], v[10:11], 0, s[2:3]
	v_readfirstlane_b32 s4, v15
	s_mov_b32 m0, s4
	s_nop 0
	global_load_lds_dwordx4 v[12:13], off
	v_add_u32_e32 v15, 0x21000, v6
	s_mov_b64 s[2:3], 0xcc00
	v_lshl_add_u64 v[12:13], v[10:11], 0, s[2:3]
	v_readfirstlane_b32 s4, v15
	s_mov_b32 m0, s4
	s_nop 0
	global_load_lds_dwordx4 v[12:13], off
	v_or_b32_e32 v12, 0x90, v27
	v_min_u32_e32 v12, 0x91, v12
	v_lshlrev_b32_e32 v12, 10, v12
	v_mov_b32_e32 v13, v109
	s_nop 0
	v_readfirstlane_b32 s4, v12
	v_lshl_add_u64 v[12:13], v[4:5], 0, v[12:13]
	s_mov_b32 s2, 0xfffebc00
	s_mov_b32 s3, -1
	v_lshl_add_u64 v[12:13], v[12:13], 0, s[2:3]
	s_mov_b32 m0, s4
	s_nop 0
	global_load_lds_dwordx4 v[12:13], off
	s_movk_i32 s2, 0xdc00
	s_mov_b32 s3, -1
	v_lshl_add_u64 v[12:13], v[10:11], 0, s[2:3]
	s_mov_b64 s[2:3], 0x12000
	v_lshl_add_u64 v[142:143], v[8:9], 0, s[2:3]
	s_movk_i32 s4, 0x23f
	v_cmp_lt_u32_e32 vcc, s4, v0
	v_add_u32_e32 v15, 0x12000, v6
	s_nop 0
	v_cndmask_b32_e32 v12, v142, v12, vcc
	v_cndmask_b32_e32 v13, v143, v13, vcc
	v_readfirstlane_b32 s4, v15
	s_mov_b32 m0, s4
	s_nop 0
	global_load_lds_dwordx4 v[12:13], off
	v_mov_b32_e32 v15, v6
	v_mov_b32_e32 v12, v8
	v_mov_b32_e32 v13, v9
	v_readfirstlane_b32 s4, v15
	s_mov_b32 m0, s4
	s_nop 0
	global_load_lds_dwordx4 v[12:13], off
	v_add_u32_e32 v15, 0x3000, v6
	s_mov_b64 s[2:3], 0x3000
	v_lshl_add_u64 v[12:13], v[8:9], 0, s[2:3]
	v_readfirstlane_b32 s4, v15
	s_mov_b32 m0, s4
	s_nop 0
	global_load_lds_dwordx4 v[12:13], off
	v_add_u32_e32 v15, 0x6000, v6
	s_mov_b64 s[2:3], 0x6000
	v_lshl_add_u64 v[12:13], v[8:9], 0, s[2:3]
	v_readfirstlane_b32 s4, v15
	s_mov_b32 m0, s4
	s_nop 0
	global_load_lds_dwordx4 v[12:13], off
	v_add_u32_e32 v15, 0x9000, v6
	s_mov_b64 s[2:3], 0x9000
	v_lshl_add_u64 v[12:13], v[8:9], 0, s[2:3]
	v_readfirstlane_b32 s4, v15
	s_mov_b32 m0, s4
	s_nop 0
	global_load_lds_dwordx4 v[12:13], off
	v_add_u32_e32 v15, 0xc000, v6
	s_mov_b64 s[2:3], 0xc000
	v_lshl_add_u64 v[12:13], v[8:9], 0, s[2:3]
	v_readfirstlane_b32 s4, v15
	s_mov_b32 m0, s4
	s_nop 0
	global_load_lds_dwordx4 v[12:13], off
	v_add_u32_e32 v15, 0xf000, v6
	s_mov_b64 s[2:3], 0xf000
	v_lshl_add_u64 v[12:13], v[8:9], 0, s[2:3]
	v_readfirstlane_b32 s4, v15
	s_mov_b32 m0, s4
	s_nop 0
	global_load_lds_dwordx4 v[12:13], off
	s_mov_b32 s2, 0x14400
	v_mul_u32_u24_e32 v4, 0x4080, v119
	s_waitcnt vmcnt(6)
	v_add3_u32 v5, v108, v4, s2
	v_lshl_or_b32 v4, v118, 2, v4
	s_mov_b64 s[2:3], 0x14280
	s_waitcnt lgkmcnt(0)
	s_barrier
	v_add_u32_e32 v4, 0x18400, v4
	v_lshl_add_u64 v[2:3], v[2:3], 0, s[2:3]
	ds_read_b128 v[88:91], v5
	ds_read_b128 v[84:87], v5 offset:1024
	ds_read_b128 v[80:83], v5 offset:2048
	ds_read_b128 v[76:79], v5 offset:3072
	ds_read_b128 v[72:75], v5 offset:4096
	ds_read_b128 v[68:71], v5 offset:5120
	ds_read_b128 v[64:67], v5 offset:6144
	ds_read_b128 v[60:63], v5 offset:7168
	ds_read_b128 v[56:59], v5 offset:8192
	ds_read_b128 v[52:55], v5 offset:9216
	ds_read_b128 v[48:51], v5 offset:10240
	ds_read_b128 v[44:47], v5 offset:11264
	ds_read_b128 v[40:43], v5 offset:12288
	ds_read_b128 v[36:39], v5 offset:13312
	ds_read_b128 v[32:35], v5 offset:14336
	ds_read_b128 v[28:31], v5 offset:15360
	ds_read_b32 v116, v4
	s_waitcnt lgkmcnt(0)
	v_lshl_add_u64 v[4:5], v[2:3], 0, v[6:7]
	v_add_u32_e32 v7, 0x14280, v6
	s_barrier
	v_readfirstlane_b32 s2, v7
	v_add_u32_e32 v7, 0x17280, v6
	s_mov_b32 m0, s2
	v_mov_b32_e32 v15, v109
	v_readfirstlane_b32 s2, v7
	v_add_u32_e32 v7, 0x1a280, v6
	global_load_lds_dwordx4 v[4:5], off
	v_lshl_add_u64 v[4:5], v[2:3], 0, v[14:15]
	s_mov_b32 m0, s2
	v_mov_b32_e32 v17, v109
	v_readfirstlane_b32 s2, v7
	v_add_u32_e32 v7, 0x1d280, v6
	global_load_lds_dwordx4 v[4:5], off
	v_lshl_add_u64 v[4:5], v[2:3], 0, v[16:17]
	s_mov_b32 m0, s2
	v_mov_b32_e32 v19, v109
	v_readfirstlane_b32 s2, v7
	global_load_lds_dwordx4 v[4:5], off
	v_lshl_add_u64 v[4:5], v[2:3], 0, v[18:19]
	s_mov_b32 m0, s2
	v_bfe_u32 v117, v0, 5, 1
	global_load_lds_dwordx4 v[4:5], off
	v_or_b32_e32 v4, 0xc000, v6
	v_add_u32_e32 v6, 0x20280, v6
	v_mov_b32_e32 v5, v109
	v_readfirstlane_b32 s2, v6
	v_lshl_add_u64 v[4:5], v[2:3], 0, v[4:5]
	s_mov_b32 m0, s2
	v_add_u32_e32 v131, 33, v115
	global_load_lds_dwordx4 v[4:5], off
	v_min_u32_e32 v4, 4, v27
	v_lshlrev_b32_e32 v6, 10, v4
	v_add_u32_e32 v4, 0xf000, v6
	v_mov_b32_e32 v5, v109
	v_lshl_add_u64 v[2:3], v[2:3], 0, v[4:5]
	v_add_u32_e32 v4, 0x23280, v6
	s_movk_i32 s73, 0x4080
	v_readfirstlane_b32 s2, v4
	s_mov_b32 m0, s2
	v_mov_b32_e32 v18, 0x7f800000
	global_load_lds_dwordx4 v[2:3], off
	v_lshrrev_b32_e32 v2, 1, v0
	v_and_b32_e32 v3, 3, v0
	v_and_or_b32 v2, v2, 12, v3
	v_cmp_eq_u32_e64 s[2:3], 0, v2
	v_cmp_eq_u32_e64 s[4:5], 1, v2
	v_cmp_eq_u32_e64 s[6:7], 2, v2
	v_cmp_eq_u32_e64 s[8:9], 3, v2
	v_cmp_eq_u32_e64 s[10:11], 4, v2
	v_cmp_eq_u32_e64 s[12:13], 5, v2
	v_cmp_eq_u32_e64 s[14:15], 6, v2
	v_cmp_eq_u32_e64 s[16:17], 7, v2
	v_cmp_eq_u32_e64 s[18:19], 8, v2
	v_cmp_eq_u32_e64 s[20:21], 9, v2
	v_cmp_eq_u32_e64 s[22:23], 10, v2
	v_cmp_eq_u32_e64 s[24:25], 11, v2
	v_cmp_eq_u32_e64 s[26:27], 12, v2
	v_cmp_eq_u32_e64 s[28:29], 13, v2
	v_cmp_eq_u32_e64 s[30:31], 14, v2
	v_cmp_eq_u32_e64 s[34:35], 15, v2
	v_mul_u32_u24_e32 v2, 0x4080, v115
	v_lshl_or_b32 v2, v117, 4, v2
	v_bfe_u32 v3, v0, 2, 1
	v_add_u32_e32 v132, 0x4000, v2
	v_lshl_or_b32 v2, s59, 2, v119
	v_cmp_eq_u32_e32 vcc, v117, v3
	v_sub_u32_e32 v3, s78, v115
	v_sub_u32_e32 v134, v2, v115
	v_add_u32_e32 v2, s72, v131
	v_cmp_lt_i32_e64 s[36:37], 0, v3
	v_cmp_lt_i32_e64 s[38:39], 3, v3
	v_cmp_lt_i32_e64 s[40:41], 6, v3
	v_cmp_lt_i32_e64 s[42:43], 9, v3
	v_cmp_lt_i32_e64 s[44:45], 12, v3
	v_cmp_lt_i32_e64 s[46:47], 15, v3
	v_cmp_lt_i32_e64 s[48:49], 18, v3
	v_cmp_lt_i32_e64 s[50:51], 21, v3
	v_cmp_lt_i32_e64 s[52:53], 24, v3
	v_cmp_lt_i32_e64 s[54:55], 27, v3
	v_cmp_lt_i32_e64 s[56:57], 30, v3
	v_ashrrev_i32_e32 v3, 31, v2
	v_lshlrev_b64 v[2:3], 10, v[2:3]
	v_lshl_or_b32 v2, v1, 2, v2
	v_lshl_add_u64 v[110:111], s[0:1], 0, v[108:109]
	v_cmp_gt_i32_e64 s[0:1], s78, v131
	s_and_b64 s[2:3], vcc, s[2:3]
	s_and_b64 s[4:5], vcc, s[4:5]
	s_and_b64 s[6:7], vcc, s[6:7]
	s_and_b64 s[8:9], vcc, s[8:9]
	s_and_b64 s[10:11], vcc, s[10:11]
	s_and_b64 s[12:13], vcc, s[12:13]
	s_and_b64 s[14:15], vcc, s[14:15]
	s_and_b64 s[16:17], vcc, s[16:17]
	s_and_b64 s[18:19], vcc, s[18:19]
	s_and_b64 s[20:21], vcc, s[20:21]
	s_and_b64 s[22:23], vcc, s[22:23]
	s_and_b64 s[24:25], vcc, s[24:25]
	s_and_b64 s[26:27], vcc, s[26:27]
	s_and_b64 s[28:29], vcc, s[28:29]
	s_and_b64 s[30:31], vcc, s[30:31]
	s_and_b64 s[34:35], vcc, s[34:35]
	v_mad_u32_u24 v133, v115, s73, v108
	v_lshl_add_u64 v[112:113], s[60:61], 0, v[2:3]
	s_mov_b64 s[60:61], -1
	v_mov_b32_e32 v135, 0x4080
	v_mov_b32_e32 v136, 0xff800000
	v_mov_b32_e32 v137, 0
	s_mov_b32 s81, s79
	v_mov_b32_e32 v1, v18
	v_mov_b32_e32 v20, v18
	v_mov_b32_e32 v19, v18
	v_mov_b32_e32 v24, v18
	v_mov_b32_e32 v23, v18
	v_mov_b32_e32 v22, v18
	v_mov_b32_e32 v21, v18
	v_mov_b32_e32 v26, v18
	v_mov_b32_e32 v25, v18
	s_waitcnt vmcnt(7)
	s_barrier
	s_branch .LBB1_6

.LBB1_12:
	s_cmp_eq_u32 s82, 0
	s_cselect_b64 s[72:73], -1, 0
	v_cndmask_b32_e64 v2, 0, 1, s[72:73]
	v_cmp_eq_u32_e32 vcc, v138, v2
	s_cbranch_vccnz .LBB1_18
	s_cmp_eq_u32 s82, 0x18300
	s_cbranch_scc1 .LBB1_18
	s_cmpk_lg_u32 s82, 0xc180
	s_cselect_b64 s[74:75], -1, 0
	s_xor_b64 s[84:85], s[60:61], -1
	s_or_b64 s[74:75], s[84:85], s[74:75]
	s_mov_b64 s[72:73], -1
	s_and_b64 vcc, exec, s[74:75]
	s_cbranch_vccz .LBB1_15
	s_waitcnt vmcnt(0)
	s_mov_b64 s[72:73], 0
